# agg1: conflict-free LDS staging layout for the hinB tile
# baseline (speedup 1.0000x reference)
_Z11agg1_kernelPKDF16_PKfS2_PKiS4_S2_S2_PDF16_PfS6_i:
	s_load_dwordx8 s[4:11], s[0:1], 0x0
	s_load_dwordx8 s[12:19], s[0:1], 0x20
	s_load_dwordx4 s[20:23], s[0:1], 0x40
	s_load_dword s24, s[0:1], 0x50
	v_lshlrev_b32_e32 v32, 2, v0
	v_readfirstlane_b32 s25, v0
	s_lshl_b32 s26, s2, 5
	v_and_b32_e32 v64, 7, v0
	v_bfe_u32 v65, v0, 3, 3
	s_lshr_b32 s25, s25, 6
	s_lshl_b32 s27, s25, 3
	s_add_i32 s26, s26, s27
	v_lshlrev_b32_e32 v1, 1, v64
	v_add_u32_e32 v66, s26, v65
	s_waitcnt lgkmcnt(0)
	global_load_dword v33, v32, s[14:15]
	global_load_dword v34, v32, s[16:17]
	s_add_i32 s28, s24, -1
	v_cmp_gt_i32_e64 s[36:37], s24, v66
	v_min_i32_e32 v66, s28, v66
	v_lshlrev_b32_e32 v4, 2, v66
	global_load_dword v10, v4, s[10:11]
	global_load_dword v11, v4, s[10:11] offset:4
	v_lshlrev_b32_e32 v35, 2, v64
	v_lshl_or_b32 v35, v66, 5, v35
	global_load_dword v9, v35, s[8:9]
	s_cmp_le_i32 s24, s26
	s_waitcnt vmcnt(3)
	ds_write2st64_b32 v32, v33, v34 offset0:32 offset1:36
	s_waitcnt lgkmcnt(0)
	s_barrier
	s_cbranch_scc1 .Lagg_exit
	v_lshlrev_b32_e32 v3, 4, v64
	v_lshl_add_u32 v3, v65, 1, v3
	s_lshl_b32 s27, s25, 11
	v_add_u32_e32 v3, s27, v3
	v_lshlrev_b32_e32 v62, 6, v64
	v_add_u32_e32 v62, 0x2000, v62
	v_cmp_eq_u32_e64 s[34:35], 0, v64
	v_lshlrev_b32_e32 v32, 8, v64
	v_lshl_add_u32 v32, v65, 4, v32
	v_add_u32_e32 v63, s27, v32
	v_mov_b32_e32 v36, 0
	v_mov_b32_e32 v37, 0
	v_mov_b32_e32 v38, 0
	v_mov_b32_e32 v39, 0
	ds_write_b128 v63, v[36:39]
	ds_write_b128 v63, v[36:39] offset:128
	s_waitcnt vmcnt(1)
	v_sub_u32_e32 v11, v11, v10
	v_add_u32_e32 v11, 1, v11
	s_nop 1
	v_readlane_b32 s29, v11, 0
	v_readlane_b32 s40, v11, 8
	s_max_i32 s29, s29, s40
	v_readlane_b32 s40, v11, 16
	s_max_i32 s29, s29, s40
	v_readlane_b32 s40, v11, 24
	s_max_i32 s29, s29, s40
	v_readlane_b32 s40, v11, 32
	s_max_i32 s29, s29, s40
	v_readlane_b32 s40, v11, 40
	s_max_i32 s29, s29, s40
	v_readlane_b32 s40, v11, 48
	s_max_i32 s29, s29, s40
	v_readlane_b32 s40, v11, 56
	s_max_i32 s29, s29, s40
	v_add_u32_e32 v67, v10, v64
	v_lshlrev_b32_e32 v67, 2, v67
	v_mov_b32_e32 v5, s24
	v_mov_b32_e32 v6, s24
	v_mov_b32_e32 v7, s24
	v_mov_b32_e32 v8, s24
	v_cndmask_b32_e64 v5, v5, v66, s[34:35]
	v_cmp_gt_i32_e32 vcc, v11, v64
	s_andn2_b64 s[40:41], vcc, s[34:35]
	s_and_saveexec_b64 s[32:33], s[40:41]
	global_load_dword v5, v67, s[12:13] offset:-4
	s_mov_b64 exec, s[32:33]
	v_add_u32_e32 v68, 8, v64
	v_cmp_gt_i32_e32 vcc, v11, v68
	s_and_saveexec_b64 s[32:33], vcc
	global_load_dword v6, v67, s[12:13] offset:28
	s_mov_b64 exec, s[32:33]
	v_add_u32_e32 v68, 16, v64
	v_cmp_gt_i32_e32 vcc, v11, v68
	s_and_saveexec_b64 s[32:33], vcc
	global_load_dword v7, v67, s[12:13] offset:60
	s_mov_b64 exec, s[32:33]
	v_add_u32_e32 v68, 24, v64
	v_cmp_gt_i32_e32 vcc, v11, v68
	s_and_saveexec_b64 s[32:33], vcc
	global_load_dword v8, v67, s[12:13] offset:92
	s_mov_b64 exec, s[32:33]
	s_waitcnt vmcnt(0)
	v_lshlrev_b32_e32 v5, 4, v5
	v_lshlrev_b32_e32 v6, 4, v6
	v_lshlrev_b32_e32 v7, 4, v7
	v_lshlrev_b32_e32 v8, 4, v8
	s_mov_b32 s42, 0
	s_mov_b32 s43, 0
	s_cmp_lt_i32 s29, 3
	s_cbranch_scc1 .Lagg_first_half
	ds_swizzle_b32 v32, v5 offset:swizzle(BITMASK_PERM, "pp000")
	ds_swizzle_b32 v33, v5 offset:swizzle(BITMASK_PERM, "pp001")
	ds_swizzle_b32 v34, v5 offset:swizzle(BITMASK_PERM, "pp010")
	ds_swizzle_b32 v35, v5 offset:swizzle(BITMASK_PERM, "pp011")
	s_waitcnt lgkmcnt(0)
	v_or_b32_e32 v32, v32, v1
	v_or_b32_e32 v33, v33, v1
	v_or_b32_e32 v34, v34, v1
	v_or_b32_e32 v35, v35, v1
	global_load_ushort v36, v32, s[6:7]
	global_load_ushort v37, v33, s[6:7]
	global_load_ushort v38, v34, s[6:7]
	global_load_ushort v39, v35, s[6:7]
	v_lshlrev_b32_e32 v32, 3, v32
	v_lshlrev_b32_e32 v33, 3, v33
	v_lshlrev_b32_e32 v34, 3, v34
	v_lshlrev_b32_e32 v35, 3, v35
	global_load_dwordx4 v[40:43], v32, s[4:5]
	global_load_dwordx4 v[44:47], v33, s[4:5]
	global_load_dwordx4 v[48:51], v34, s[4:5]
	global_load_dwordx4 v[52:55], v35, s[4:5]
	s_waitcnt vmcnt(4)
	v_fma_mix_f32 v36, v36, 1.0, v9 op_sel_hi:[1,0,0]
	v_fma_mix_f32 v37, v37, 1.0, v9 op_sel_hi:[1,0,0]
	v_fma_mix_f32 v38, v38, 1.0, v9 op_sel_hi:[1,0,0]
	v_fma_mix_f32 v39, v39, 1.0, v9 op_sel_hi:[1,0,0]
	v_mul_f32_e32 v58, 0x3e4ccccd, v36
	v_mul_f32_e32 v59, 0x3e4ccccd, v37
	v_mul_f32_e32 v60, 0x3e4ccccd, v38
	v_mul_f32_e32 v61, 0x3e4ccccd, v39
	v_max_f32_e32 v36, v36, v58
	v_max_f32_e32 v37, v37, v59
	v_max_f32_e32 v38, v38, v60
	v_max_f32_e32 v39, v39, v61
	v_max3_f32 v56, v36, v37, v38
	v_max_f32_e32 v13, v56, v39
	v_sub_f32_e32 v36, v36, v13
	v_sub_f32_e32 v37, v37, v13
	v_sub_f32_e32 v38, v38, v13
	v_sub_f32_e32 v39, v39, v13
	v_exp_f32_e32 v36, v36
	v_exp_f32_e32 v37, v37
	v_exp_f32_e32 v38, v38
	v_exp_f32_e32 v39, v39
	s_nop 0
	v_add_f32_e32 v14, v36, v37
	v_add_f32_e32 v14, v14, v38
	v_add_f32_e32 v14, v14, v39
	s_waitcnt vmcnt(3)
	v_cvt_scalef32_pk_f16_fp8 v58, v40, 1.0
	v_cvt_scalef32_pk_f16_fp8 v59, v40, 1.0 op_sel:[1,0,0]
	v_cvt_scalef32_pk_f16_fp8 v60, v41, 1.0
	v_cvt_scalef32_pk_f16_fp8 v61, v41, 1.0 op_sel:[1,0,0]
	v_fma_mix_f32 v16, v58, v36, 0 op_sel_hi:[1,0,0]
	v_fma_mix_f32 v17, v58, v36, 0 op_sel:[1,0,0] op_sel_hi:[1,0,0]
	v_fma_mix_f32 v18, v59, v36, 0 op_sel_hi:[1,0,0]
	v_fma_mix_f32 v19, v59, v36, 0 op_sel:[1,0,0] op_sel_hi:[1,0,0]
	v_fma_mix_f32 v20, v60, v36, 0 op_sel_hi:[1,0,0]
	v_fma_mix_f32 v21, v60, v36, 0 op_sel:[1,0,0] op_sel_hi:[1,0,0]
	v_fma_mix_f32 v22, v61, v36, 0 op_sel_hi:[1,0,0]
	v_fma_mix_f32 v23, v61, v36, 0 op_sel:[1,0,0] op_sel_hi:[1,0,0]
	v_cvt_scalef32_pk_f16_fp8 v58, v42, 1.0
	v_cvt_scalef32_pk_f16_fp8 v59, v42, 1.0 op_sel:[1,0,0]
	v_cvt_scalef32_pk_f16_fp8 v60, v43, 1.0
	v_cvt_scalef32_pk_f16_fp8 v61, v43, 1.0 op_sel:[1,0,0]
	v_fma_mix_f32 v24, v58, v36, 0 op_sel_hi:[1,0,0]
	v_fma_mix_f32 v25, v58, v36, 0 op_sel:[1,0,0] op_sel_hi:[1,0,0]
	v_fma_mix_f32 v26, v59, v36, 0 op_sel_hi:[1,0,0]
	v_fma_mix_f32 v27, v59, v36, 0 op_sel:[1,0,0] op_sel_hi:[1,0,0]
	v_fma_mix_f32 v28, v60, v36, 0 op_sel_hi:[1,0,0]
	v_fma_mix_f32 v29, v60, v36, 0 op_sel:[1,0,0] op_sel_hi:[1,0,0]
	v_fma_mix_f32 v30, v61, v36, 0 op_sel_hi:[1,0,0]
	v_fma_mix_f32 v31, v61, v36, 0 op_sel:[1,0,0] op_sel_hi:[1,0,0]
	s_waitcnt vmcnt(2)
	v_cvt_scalef32_pk_f16_fp8 v58, v44, 1.0
	v_cvt_scalef32_pk_f16_fp8 v59, v44, 1.0 op_sel:[1,0,0]
	v_cvt_scalef32_pk_f16_fp8 v60, v45, 1.0
	v_cvt_scalef32_pk_f16_fp8 v61, v45, 1.0 op_sel:[1,0,0]
	v_fma_mix_f32 v16, v58, v37, v16 op_sel_hi:[1,0,0]
	v_fma_mix_f32 v17, v58, v37, v17 op_sel:[1,0,0] op_sel_hi:[1,0,0]
	v_fma_mix_f32 v18, v59, v37, v18 op_sel_hi:[1,0,0]
	v_fma_mix_f32 v19, v59, v37, v19 op_sel:[1,0,0] op_sel_hi:[1,0,0]
	v_fma_mix_f32 v20, v60, v37, v20 op_sel_hi:[1,0,0]
	v_fma_mix_f32 v21, v60, v37, v21 op_sel:[1,0,0] op_sel_hi:[1,0,0]
	v_fma_mix_f32 v22, v61, v37, v22 op_sel_hi:[1,0,0]
	v_fma_mix_f32 v23, v61, v37, v23 op_sel:[1,0,0] op_sel_hi:[1,0,0]
	v_cvt_scalef32_pk_f16_fp8 v58, v46, 1.0
	v_cvt_scalef32_pk_f16_fp8 v59, v46, 1.0 op_sel:[1,0,0]
	v_cvt_scalef32_pk_f16_fp8 v60, v47, 1.0
	v_cvt_scalef32_pk_f16_fp8 v61, v47, 1.0 op_sel:[1,0,0]
	v_fma_mix_f32 v24, v58, v37, v24 op_sel_hi:[1,0,0]
	v_fma_mix_f32 v25, v58, v37, v25 op_sel:[1,0,0] op_sel_hi:[1,0,0]
	v_fma_mix_f32 v26, v59, v37, v26 op_sel_hi:[1,0,0]
	v_fma_mix_f32 v27, v59, v37, v27 op_sel:[1,0,0] op_sel_hi:[1,0,0]
	v_fma_mix_f32 v28, v60, v37, v28 op_sel_hi:[1,0,0]
	v_fma_mix_f32 v29, v60, v37, v29 op_sel:[1,0,0] op_sel_hi:[1,0,0]
	v_fma_mix_f32 v30, v61, v37, v30 op_sel_hi:[1,0,0]
	v_fma_mix_f32 v31, v61, v37, v31 op_sel:[1,0,0] op_sel_hi:[1,0,0]
	s_waitcnt vmcnt(1)
	v_cvt_scalef32_pk_f16_fp8 v58, v48, 1.0
	v_cvt_scalef32_pk_f16_fp8 v59, v48, 1.0 op_sel:[1,0,0]
	v_cvt_scalef32_pk_f16_fp8 v60, v49, 1.0
	v_cvt_scalef32_pk_f16_fp8 v61, v49, 1.0 op_sel:[1,0,0]
	v_fma_mix_f32 v16, v58, v38, v16 op_sel_hi:[1,0,0]
	v_fma_mix_f32 v17, v58, v38, v17 op_sel:[1,0,0] op_sel_hi:[1,0,0]
	v_fma_mix_f32 v18, v59, v38, v18 op_sel_hi:[1,0,0]
	v_fma_mix_f32 v19, v59, v38, v19 op_sel:[1,0,0] op_sel_hi:[1,0,0]
	v_fma_mix_f32 v20, v60, v38, v20 op_sel_hi:[1,0,0]
	v_fma_mix_f32 v21, v60, v38, v21 op_sel:[1,0,0] op_sel_hi:[1,0,0]
	v_fma_mix_f32 v22, v61, v38, v22 op_sel_hi:[1,0,0]
	v_fma_mix_f32 v23, v61, v38, v23 op_sel:[1,0,0] op_sel_hi:[1,0,0]
	v_cvt_scalef32_pk_f16_fp8 v58, v50, 1.0
	v_cvt_scalef32_pk_f16_fp8 v59, v50, 1.0 op_sel:[1,0,0]
	v_cvt_scalef32_pk_f16_fp8 v60, v51, 1.0
	v_cvt_scalef32_pk_f16_fp8 v61, v51, 1.0 op_sel:[1,0,0]
	v_fma_mix_f32 v24, v58, v38, v24 op_sel_hi:[1,0,0]
	v_fma_mix_f32 v25, v58, v38, v25 op_sel:[1,0,0] op_sel_hi:[1,0,0]
	v_fma_mix_f32 v26, v59, v38, v26 op_sel_hi:[1,0,0]
	v_fma_mix_f32 v27, v59, v38, v27 op_sel:[1,0,0] op_sel_hi:[1,0,0]
	v_fma_mix_f32 v28, v60, v38, v28 op_sel_hi:[1,0,0]
	v_fma_mix_f32 v29, v60, v38, v29 op_sel:[1,0,0] op_sel_hi:[1,0,0]
	v_fma_mix_f32 v30, v61, v38, v30 op_sel_hi:[1,0,0]
	v_fma_mix_f32 v31, v61, v38, v31 op_sel:[1,0,0] op_sel_hi:[1,0,0]
	s_waitcnt vmcnt(0)
	v_cvt_scalef32_pk_f16_fp8 v58, v52, 1.0
	v_cvt_scalef32_pk_f16_fp8 v59, v52, 1.0 op_sel:[1,0,0]
	v_cvt_scalef32_pk_f16_fp8 v60, v53, 1.0
	v_cvt_scalef32_pk_f16_fp8 v61, v53, 1.0 op_sel:[1,0,0]
	v_fma_mix_f32 v16, v58, v39, v16 op_sel_hi:[1,0,0]
	v_fma_mix_f32 v17, v58, v39, v17 op_sel:[1,0,0] op_sel_hi:[1,0,0]
	v_fma_mix_f32 v18, v59, v39, v18 op_sel_hi:[1,0,0]
	v_fma_mix_f32 v19, v59, v39, v19 op_sel:[1,0,0] op_sel_hi:[1,0,0]
	v_fma_mix_f32 v20, v60, v39, v20 op_sel_hi:[1,0,0]
	v_fma_mix_f32 v21, v60, v39, v21 op_sel:[1,0,0] op_sel_hi:[1,0,0]
	v_fma_mix_f32 v22, v61, v39, v22 op_sel_hi:[1,0,0]
	v_fma_mix_f32 v23, v61, v39, v23 op_sel:[1,0,0] op_sel_hi:[1,0,0]
	v_cvt_scalef32_pk_f16_fp8 v58, v54, 1.0
	v_cvt_scalef32_pk_f16_fp8 v59, v54, 1.0 op_sel:[1,0,0]
	v_cvt_scalef32_pk_f16_fp8 v60, v55, 1.0
	v_cvt_scalef32_pk_f16_fp8 v61, v55, 1.0 op_sel:[1,0,0]
	v_fma_mix_f32 v24, v58, v39, v24 op_sel_hi:[1,0,0]
	v_fma_mix_f32 v25, v58, v39, v25 op_sel:[1,0,0] op_sel_hi:[1,0,0]
	v_fma_mix_f32 v26, v59, v39, v26 op_sel_hi:[1,0,0]
	v_fma_mix_f32 v27, v59, v39, v27 op_sel:[1,0,0] op_sel_hi:[1,0,0]
	v_fma_mix_f32 v28, v60, v39, v28 op_sel_hi:[1,0,0]
	v_fma_mix_f32 v29, v60, v39, v29 op_sel:[1,0,0] op_sel_hi:[1,0,0]
	v_fma_mix_f32 v30, v61, v39, v30 op_sel_hi:[1,0,0]
	v_fma_mix_f32 v31, v61, v39, v31 op_sel:[1,0,0] op_sel_hi:[1,0,0]
	s_sub_i32 s29, s29, 4
	s_branch .Lagg_B

.Lagg_epi:
	s_and_saveexec_b64 s[32:33], s[36:37]
	v_rcp_f32_e32 v57, v14
	ds_read_b128 v[32:35], v62 offset:0
	ds_read_b128 v[36:39], v62 offset:16
	ds_read_b128 v[40:43], v62 offset:512
	ds_read_b128 v[44:47], v62 offset:528
	ds_read_b128 v[48:51], v62 offset:1024
	ds_read_b128 v[52:55], v62 offset:1040
	s_waitcnt lgkmcnt(2)
	v_mul_f32_e32 v16, v16, v57
	v_mul_f32_e32 v17, v17, v57
	v_mul_f32_e32 v18, v18, v57
	v_mul_f32_e32 v19, v19, v57
	v_mul_f32_e32 v20, v20, v57
	v_mul_f32_e32 v21, v21, v57
	v_mul_f32_e32 v22, v22, v57
	v_mul_f32_e32 v23, v23, v57
	v_fma_f32 v16, v16, v32, v40
	v_fma_f32 v17, v17, v33, v41
	v_fma_f32 v18, v18, v34, v42
	v_fma_f32 v19, v19, v35, v43
	v_fma_f32 v20, v20, v36, v44
	v_fma_f32 v21, v21, v37, v45
	v_fma_f32 v22, v22, v38, v46
	v_fma_f32 v23, v23, v39, v47
	ds_read_b128 v[32:35], v62 offset:1536
	ds_read_b128 v[36:39], v62 offset:1552
	v_mul_f32_e32 v59, 0x3fb8aa3b, v16
	v_mul_f32_e32 v60, 0x3fb8aa3b, v17
	v_mul_f32_e32 v61, 0x3fb8aa3b, v18
	v_mul_f32_e32 v67, 0x3fb8aa3b, v19
	v_exp_f32_e32 v59, v59
	v_exp_f32_e32 v60, v60
	v_exp_f32_e32 v61, v61
	v_exp_f32_e32 v67, v67
	v_add_f32_e32 v59, -1.0, v59
	v_add_f32_e32 v60, -1.0, v60
	v_add_f32_e32 v61, -1.0, v61
	v_add_f32_e32 v67, -1.0, v67
	v_med3_f32 v16, v16, v59, 0
	v_med3_f32 v17, v17, v60, 0
	v_med3_f32 v18, v18, v61, 0
	v_med3_f32 v19, v19, v67, 0
	v_cvt_f16_f32_e32 v59, v16
	v_cvt_f16_f32_e32 v60, v17
	v_cvt_f16_f32_e32 v61, v18
	v_cvt_f16_f32_e32 v67, v19
	ds_write_b16 v3, v59
	ds_write_b16 v3, v60 offset:128
	ds_write_b16 v3, v61 offset:256
	ds_write_b16 v3, v67 offset:384
	v_mul_f32_e32 v59, 0x3fb8aa3b, v20
	v_mul_f32_e32 v60, 0x3fb8aa3b, v21
	v_mul_f32_e32 v61, 0x3fb8aa3b, v22
	v_mul_f32_e32 v67, 0x3fb8aa3b, v23
	v_exp_f32_e32 v59, v59
	v_exp_f32_e32 v60, v60
	v_exp_f32_e32 v61, v61
	v_exp_f32_e32 v67, v67
	v_add_f32_e32 v59, -1.0, v59
	v_add_f32_e32 v60, -1.0, v60
	v_add_f32_e32 v61, -1.0, v61
	v_add_f32_e32 v67, -1.0, v67
	v_med3_f32 v20, v20, v59, 0
	v_med3_f32 v21, v21, v60, 0
	v_med3_f32 v22, v22, v61, 0
	v_med3_f32 v23, v23, v67, 0
	v_cvt_f16_f32_e32 v59, v20
	v_cvt_f16_f32_e32 v60, v21
	v_cvt_f16_f32_e32 v61, v22
	v_cvt_f16_f32_e32 v67, v23
	ds_write_b16 v3, v59 offset:512
	ds_write_b16 v3, v60 offset:640
	ds_write_b16 v3, v61 offset:768
	ds_write_b16 v3, v67 offset:896
	s_waitcnt lgkmcnt(0)
	v_mul_f32_e32 v56, v16, v48
	v_mul_f32_e32 v58, v16, v32
	v_fmac_f32_e32 v56, v17, v49
	v_fmac_f32_e32 v58, v17, v33
	v_fmac_f32_e32 v56, v18, v50
	v_fmac_f32_e32 v58, v18, v34
	v_fmac_f32_e32 v56, v19, v51
	v_fmac_f32_e32 v58, v19, v35
	v_fmac_f32_e32 v56, v20, v52
	v_fmac_f32_e32 v58, v20, v36
	v_fmac_f32_e32 v56, v21, v53
	v_fmac_f32_e32 v58, v21, v37
	v_fmac_f32_e32 v56, v22, v54
	v_fmac_f32_e32 v58, v22, v38
	v_fmac_f32_e32 v56, v23, v55
	v_fmac_f32_e32 v58, v23, v39
	ds_read_b128 v[32:35], v62 offset:32
	ds_read_b128 v[36:39], v62 offset:48
	ds_read_b128 v[40:43], v62 offset:544
	ds_read_b128 v[44:47], v62 offset:560
	ds_read_b128 v[48:51], v62 offset:1056
	ds_read_b128 v[52:55], v62 offset:1072
	s_waitcnt lgkmcnt(2)
	v_mul_f32_e32 v24, v24, v57
	v_mul_f32_e32 v25, v25, v57
	v_mul_f32_e32 v26, v26, v57
	v_mul_f32_e32 v27, v27, v57
	v_mul_f32_e32 v28, v28, v57
	v_mul_f32_e32 v29, v29, v57
	v_mul_f32_e32 v30, v30, v57
	v_mul_f32_e32 v31, v31, v57
	v_fma_f32 v24, v24, v32, v40
	v_fma_f32 v25, v25, v33, v41
	v_fma_f32 v26, v26, v34, v42
	v_fma_f32 v27, v27, v35, v43
	v_fma_f32 v28, v28, v36, v44
	v_fma_f32 v29, v29, v37, v45
	v_fma_f32 v30, v30, v38, v46
	v_fma_f32 v31, v31, v39, v47
	ds_read_b128 v[32:35], v62 offset:1568
	ds_read_b128 v[36:39], v62 offset:1584
	v_mul_f32_e32 v59, 0x3fb8aa3b, v24
	v_mul_f32_e32 v60, 0x3fb8aa3b, v25
	v_mul_f32_e32 v61, 0x3fb8aa3b, v26
	v_mul_f32_e32 v67, 0x3fb8aa3b, v27
	v_exp_f32_e32 v59, v59
	v_exp_f32_e32 v60, v60
	v_exp_f32_e32 v61, v61
	v_exp_f32_e32 v67, v67
	v_add_f32_e32 v59, -1.0, v59
	v_add_f32_e32 v60, -1.0, v60
	v_add_f32_e32 v61, -1.0, v61
	v_add_f32_e32 v67, -1.0, v67
	v_med3_f32 v24, v24, v59, 0
	v_med3_f32 v25, v25, v60, 0
	v_med3_f32 v26, v26, v61, 0
	v_med3_f32 v27, v27, v67, 0
	v_cvt_f16_f32_e32 v59, v24
	v_cvt_f16_f32_e32 v60, v25
	v_cvt_f16_f32_e32 v61, v26
	v_cvt_f16_f32_e32 v67, v27
	ds_write_b16 v3, v59 offset:1024
	ds_write_b16 v3, v60 offset:1152
	ds_write_b16 v3, v61 offset:1280
	ds_write_b16 v3, v67 offset:1408
	v_mul_f32_e32 v59, 0x3fb8aa3b, v28
	v_mul_f32_e32 v60, 0x3fb8aa3b, v29
	v_mul_f32_e32 v61, 0x3fb8aa3b, v30
	v_mul_f32_e32 v67, 0x3fb8aa3b, v31
	v_exp_f32_e32 v59, v59
	v_exp_f32_e32 v60, v60
	v_exp_f32_e32 v61, v61
	v_exp_f32_e32 v67, v67
	v_add_f32_e32 v59, -1.0, v59
	v_add_f32_e32 v60, -1.0, v60
	v_add_f32_e32 v61, -1.0, v61
	v_add_f32_e32 v67, -1.0, v67
	v_med3_f32 v28, v28, v59, 0
	v_med3_f32 v29, v29, v60, 0
	v_med3_f32 v30, v30, v61, 0
	v_med3_f32 v31, v31, v67, 0
	v_cvt_f16_f32_e32 v59, v28
	v_cvt_f16_f32_e32 v60, v29
	v_cvt_f16_f32_e32 v61, v30
	v_cvt_f16_f32_e32 v67, v31
	ds_write_b16 v3, v59 offset:1536
	ds_write_b16 v3, v60 offset:1664
	ds_write_b16 v3, v61 offset:1792
	ds_write_b16 v3, v67 offset:1920
	s_waitcnt lgkmcnt(0)
	v_fmac_f32_e32 v56, v24, v48
	v_fmac_f32_e32 v58, v24, v32
	v_fmac_f32_e32 v56, v25, v49
	v_fmac_f32_e32 v58, v25, v33
	v_fmac_f32_e32 v56, v26, v50
	v_fmac_f32_e32 v58, v26, v34
	v_fmac_f32_e32 v56, v27, v51
	v_fmac_f32_e32 v58, v27, v35
	v_fmac_f32_e32 v56, v28, v52
	v_fmac_f32_e32 v58, v28, v36
	v_fmac_f32_e32 v56, v29, v53
	v_fmac_f32_e32 v58, v29, v37
	v_fmac_f32_e32 v56, v30, v54
	v_fmac_f32_e32 v58, v30, v38
	v_fmac_f32_e32 v56, v31, v55
	v_fmac_f32_e32 v58, v31, v39
	s_nop 1
	v_add_f32_dpp v56, v56, v56 quad_perm:[1,0,3,2] row_mask:0xf bank_mask:0xf
	v_add_f32_dpp v58, v58, v58 quad_perm:[1,0,3,2] row_mask:0xf bank_mask:0xf
	s_nop 0
	v_add_f32_dpp v56, v56, v56 quad_perm:[2,3,0,1] row_mask:0xf bank_mask:0xf
	v_add_f32_dpp v58, v58, v58 quad_perm:[2,3,0,1] row_mask:0xf bank_mask:0xf
	s_nop 0
	ds_swizzle_b32 v59, v56 offset:swizzle(SWAP,4)
	ds_swizzle_b32 v60, v58 offset:swizzle(SWAP,4)
	s_waitcnt lgkmcnt(0)
	v_add_f32_e32 v56, v56, v59
	v_add_f32_e32 v58, v58, v60
	s_and_b64 exec, exec, s[34:35]
	global_store_dword v4, v56, s[20:21]
	global_store_dword v4, v58, s[22:23]
	s_mov_b64 exec, s[32:33]
	s_waitcnt lgkmcnt(0)
	ds_read_b128 v[32:35], v63
	ds_read_b128 v[36:39], v63 offset:128
	s_ashr_i32 s27, s26, 3
	s_lshl_b32 s27, s27, 11
	v_and_b32_e32 v40, 63, v0
	v_lshlrev_b32_e32 v40, 5, v40
	v_add_u32_e32 v40, s27, v40
	s_waitcnt lgkmcnt(0)
	global_store_dwordx4 v40, v[32:35], s[18:19]
	global_store_dwordx4 v40, v[36:39], s[18:19] offset:16
